# grid barrier: the last XCD leader releases every XCD's generation word itself (one hop fewer); other leaders wait on their XCD word
# speedup vs baseline: 1.0073x; 1.0036x over previous
.LBB0_187:
	s_or_b64 exec, exec, s[6:7]
	s_waitcnt vmcnt(0)
	v_readfirstlane_b32 s4, v4
	v_sub_u32_e32 v5, 0, v2
	s_mov_b64 s[6:7], -1
	v_add_u32_e32 v4, s4, v1
	v_cvt_f32_u32_e32 v1, v2
	v_readlane_b32 s4, v253, 14
	v_readlane_b32 s5, v253, 15
	v_rcp_iflag_f32_e32 v1, v1
	s_nop 0
	v_mul_f32_e32 v1, 0x4f7ffffe, v1
	v_cvt_u32_f32_e32 v1, v1
	v_mul_lo_u32 v5, v5, v1
	v_mul_hi_u32 v5, v1, v5
	v_add_u32_e32 v1, v1, v5
	v_mul_hi_u32 v1, v4, v1
	v_mul_lo_u32 v5, v1, v2
	v_sub_u32_e32 v5, v4, v5
	v_cmp_ge_u32_e32 vcc, v5, v2
	v_add_u32_e32 v6, 1, v1
	v_add_u32_e32 v4, 1, v4
	v_cndmask_b32_e32 v1, v1, v6, vcc
	v_sub_u32_e32 v6, v5, v2
	v_cndmask_b32_e32 v5, v5, v6, vcc
	v_cmp_ge_u32_e32 vcc, v5, v2
	v_add_u32_e32 v5, 1, v1
	s_nop 0
	v_cndmask_b32_e32 v1, v1, v5, vcc
	v_mul_lo_u32 v5, v2, v1
	v_add_u32_e32 v2, v5, v2
	v_cmp_ne_u32_e32 vcc, v4, v2
	v_mov_b64_e32 v[4:5], s[4:5]
	s_and_saveexec_b64 s[4:5], vcc
	s_cbranch_execz .LBB0_199
	v_readlane_b32 s6, v253, 10
	v_readlane_b32 s7, v253, 11
	s_mov_b64 s[8:9], 0
	s_nop 3
	global_load_dword v2, v3, s[6:7] sc1
	s_waitcnt vmcnt(0)
	v_cmp_eq_u32_e32 vcc, v2, v1
	s_and_saveexec_b64 s[6:7], vcc
	s_cbranch_execz .LBB0_198
	s_mov_b32 s40, 1
	s_branch .LBB0_191

.LBB0_199:
	s_mov_b32 s15, 0
	s_or_b64 exec, exec, s[4:5]
	s_and_saveexec_b64 s[4:5], s[6:7]
	s_cbranch_execz .LBB0_201
	global_atomic_add v[4:5], v228, off
	s_mov_b32 s15, 1
	v_readlane_b32 s10, v253, 14
	v_readfirstlane_b32 s11, v4
	s_cmp_lg_u32 s10, s11
	s_cbranch_scc1 .Lbx_done_0
	s_mov_b32 s15, 0
	s_add_u32 s12, s16, 0x6400
	s_addc_u32 s13, s17, 0
	s_mov_b32 s14, 16
.Lbx_loop_0:
	global_atomic_add v3, v228, s[12:13]
	s_add_u32 s12, s12, 0x100
	s_addc_u32 s13, s13, 0
	s_sub_u32 s14, s14, 1
	s_cmp_lg_u32 s14, 0
	s_cbranch_scc1 .Lbx_loop_0
.Lbx_done_0:
.LBB0_201:
	s_or_b64 exec, exec, s[4:5]
	v_readlane_b32 s4, v253, 10
	v_readlane_b32 s5, v253, 11
	s_waitcnt vmcnt(0)
	s_nop 0
	s_nop 2
	s_cmp_eq_u32 s15, 0
	s_cbranch_scc1 .Lbx_noown_0
	global_atomic_add v3, v228, s[4:5]
.Lbx_noown_0:
	s_waitcnt vmcnt(0)
.LBB0_202:
	s_or_b64 exec, exec, s[2:3]
	s_waitcnt lgkmcnt(0)
	s_barrier

.Lbx_noown_1:
	s_waitcnt vmcnt(0)
.LBB0_276:
	s_or_b64 exec, exec, s[2:3]
	s_waitcnt lgkmcnt(0)
	s_barrier

.LBB0_337:
	s_or_b64 exec, exec, s[6:7]
	s_waitcnt vmcnt(0)
	v_readfirstlane_b32 s4, v4
	v_sub_u32_e32 v5, 0, v2
	s_mov_b64 s[6:7], -1
	v_add_u32_e32 v4, s4, v1
	v_cvt_f32_u32_e32 v1, v2
	v_readlane_b32 s4, v253, 14
	v_readlane_b32 s5, v253, 15
	v_rcp_iflag_f32_e32 v1, v1
	s_nop 0
	v_mul_f32_e32 v1, 0x4f7ffffe, v1
	v_cvt_u32_f32_e32 v1, v1
	v_mul_lo_u32 v5, v5, v1
	v_mul_hi_u32 v5, v1, v5
	v_add_u32_e32 v1, v1, v5
	v_mul_hi_u32 v1, v4, v1
	v_mul_lo_u32 v5, v1, v2
	v_sub_u32_e32 v5, v4, v5
	v_cmp_ge_u32_e32 vcc, v5, v2
	v_add_u32_e32 v6, 1, v1
	v_add_u32_e32 v4, 1, v4
	v_cndmask_b32_e32 v1, v1, v6, vcc
	v_sub_u32_e32 v6, v5, v2
	v_cndmask_b32_e32 v5, v5, v6, vcc
	v_cmp_ge_u32_e32 vcc, v5, v2
	v_add_u32_e32 v5, 1, v1
	s_nop 0
	v_cndmask_b32_e32 v1, v1, v5, vcc
	v_mul_lo_u32 v5, v2, v1
	v_add_u32_e32 v2, v5, v2
	v_cmp_ne_u32_e32 vcc, v4, v2
	v_mov_b64_e32 v[4:5], s[4:5]
	s_and_saveexec_b64 s[4:5], vcc
	s_cbranch_execz .LBB0_349
	v_readlane_b32 s6, v253, 10
	v_readlane_b32 s7, v253, 11
	s_mov_b64 s[8:9], 0
	s_nop 3
	global_load_dword v2, v3, s[6:7] sc1
	s_waitcnt vmcnt(0)
	v_cmp_eq_u32_e32 vcc, v2, v1
	s_and_saveexec_b64 s[6:7], vcc
	s_cbranch_execz .LBB0_348
	s_mov_b32 s33, 1
	s_branch .LBB0_341

.Lbx_noown_2:
	s_waitcnt vmcnt(0)
.LBB0_352:
	s_or_b64 exec, exec, s[2:3]
	s_waitcnt lgkmcnt(0)
	s_barrier

.LBB0_541:
	s_or_b64 exec, exec, s[6:7]
	s_waitcnt vmcnt(0)
	v_readfirstlane_b32 s4, v4
	v_sub_u32_e32 v5, 0, v2
	s_mov_b64 s[6:7], -1
	v_add_u32_e32 v4, s4, v1
	v_cvt_f32_u32_e32 v1, v2
	v_readlane_b32 s4, v253, 14
	v_readlane_b32 s5, v253, 15
	v_rcp_iflag_f32_e32 v1, v1
	s_nop 0
	v_mul_f32_e32 v1, 0x4f7ffffe, v1
	v_cvt_u32_f32_e32 v1, v1
	v_mul_lo_u32 v5, v5, v1
	v_mul_hi_u32 v5, v1, v5
	v_add_u32_e32 v1, v1, v5
	v_mul_hi_u32 v1, v4, v1
	v_mul_lo_u32 v5, v1, v2
	v_sub_u32_e32 v5, v4, v5
	v_cmp_ge_u32_e32 vcc, v5, v2
	v_add_u32_e32 v6, 1, v1
	v_add_u32_e32 v4, 1, v4
	v_cndmask_b32_e32 v1, v1, v6, vcc
	v_sub_u32_e32 v6, v5, v2
	v_cndmask_b32_e32 v5, v5, v6, vcc
	v_cmp_ge_u32_e32 vcc, v5, v2
	v_add_u32_e32 v5, 1, v1
	s_nop 0
	v_cndmask_b32_e32 v1, v1, v5, vcc
	v_mul_lo_u32 v5, v2, v1
	v_add_u32_e32 v2, v5, v2
	v_cmp_ne_u32_e32 vcc, v4, v2
	v_mov_b64_e32 v[4:5], s[4:5]
	s_and_saveexec_b64 s[4:5], vcc
	s_cbranch_execz .LBB0_553
	v_readlane_b32 s6, v253, 10
	v_readlane_b32 s7, v253, 11
	s_mov_b64 s[8:9], 0
	s_nop 3
	global_load_dword v2, v3, s[6:7] sc1
	s_waitcnt vmcnt(0)
	v_cmp_eq_u32_e32 vcc, v2, v1
	s_and_saveexec_b64 s[6:7], vcc
	s_cbranch_execz .LBB0_552
	s_mov_b32 s34, 1
	s_branch .LBB0_545

.Lbx_noown_3:
	s_waitcnt vmcnt(0)
.LBB0_556:
	s_or_b64 exec, exec, s[2:3]
	s_waitcnt lgkmcnt(0)
	s_barrier

.Lbx_noown_4:
	s_waitcnt vmcnt(0)
.LBB0_699:
	s_or_b64 exec, exec, s[2:3]
	s_waitcnt lgkmcnt(0)
	s_barrier

.Lbx_noown_5:
	s_waitcnt vmcnt(0)
.LBB0_757:
	s_or_b64 exec, exec, s[2:3]
	s_waitcnt lgkmcnt(0)
	s_barrier

.Lbx_noown_6:
	s_waitcnt vmcnt(0)
.LBB0_817:
	s_or_b64 exec, exec, s[2:3]
	s_waitcnt lgkmcnt(0)
	s_barrier

.Lbx_noown_7:
	s_waitcnt vmcnt(0)
.LBB0_893:
	s_or_b64 exec, exec, s[2:3]
	s_waitcnt lgkmcnt(0)
	s_barrier

.Lbx_noown_8:
	s_waitcnt vmcnt(0)
.LBB0_1041:
	s_or_b64 exec, exec, s[2:3]
	s_waitcnt lgkmcnt(0)
	s_barrier

.Lbx_noown_9:
	s_waitcnt vmcnt(0)
.LBB0_1507:
	s_or_b64 exec, exec, s[2:3]
	s_waitcnt lgkmcnt(0)
	s_barrier
